# LN2 loop top: token (expert, slot) words fetched in one batch of four 8-byte loads plus one batch of four meta reads (was five serialized load-wait steps)
# speedup vs baseline: 1.0116x; 1.0070x over previous
; __global__ void __launch_bounds__(NTHREADS, 2) hybrid_fwd(Args a) {
;     ...
;             for (int row0 = gw; row0 < MTOK; row0 += 2 * NGW) {
;                 int sl[2][2];
; #pragma unroll
;                 for (int rr = 0; rr < 2; ++rr) { const int row = row0 + rr * NGW; sl[rr][0] = meta[16 + tokE[row * 2]] + tokS[row * 2]; sl[rr][1] = meta[16 + tokE[row * 2 + 1]] + tokS[row * 2 + 1]; }
;                 u32x2 xw[2][8]; unsigned pw_[2][8], qw[2][8];
; #pragma unroll
;                 for (int rr = 0; rr < 2; ++rr) { const int row = row0 + rr * NGW;
; #pragma unroll
;                     for (int j = 0; j < 8; ++j) { xw[rr][j] = __builtin_nontemporal_load((const u32x2*)(X1B + (size_t)row * DM + j * 256 + lane * 4));
;                         pw_[rr][j] = __builtin_nontemporal_load((const unsigned*)(Y2 + (size_t)sl[rr][0] * DM + j * 256 + lane * 4)); qw[rr][j] = __builtin_nontemporal_load((const unsigned*)(Y2 + (size_t)sl[rr][1] * DM + j * 256 + lane * 4)); } }
.LBB0_1336:
	s_mov_b32 s22, s27
	s_mov_b32 s23, s30
	s_mov_b32 s34, s25
	s_mov_b32 s35, s26
	s_lshl_b32 s2, s18, 2
	s_add_i32 s3, s36, s18
	s_lshl_b32 s3, s3, 2
	v_mov_b32_e32 v6, s2
	v_mov_b32_e32 v7, s3
	global_load_dwordx2 v[0:1], v6, s[22:23]
	global_load_dwordx2 v[2:3], v6, s[34:35]
	global_load_dwordx2 v[4:5], v7, s[22:23]
	global_load_dwordx2 v[46:47], v7, s[34:35]
	v_lshl_add_u64 v[40:41], s[4:5], 0, v[32:33]
	s_waitcnt vmcnt(0)
	v_lshl_add_u32 v0, v0, 2, s31
	v_lshl_add_u32 v1, v1, 2, s31
	v_lshl_add_u32 v4, v4, 2, s31
	v_lshl_add_u32 v5, v5, 2, s31
	ds_read_b32 v0, v0 offset:64
	ds_read_b32 v1, v1 offset:64
	ds_read_b32 v4, v4 offset:64
	ds_read_b32 v5, v5 offset:64
	s_waitcnt lgkmcnt(0)
	v_add_u32_e32 v0, v2, v0
	v_add_u32_e32 v2, v3, v1
	v_add_u32_e32 v42, v46, v4
	v_add_u32_e32 v44, v47, v5
	s_mov_b32 s2, 0x42000000
	v_ashrrev_i32_e32 v43, 31, v42
	v_lshlrev_b64 v[42:43], 11, v[42:43]
	v_lshl_add_u64 v[70:71], v[8:9], 0, v[42:43]
	v_ashrrev_i32_e32 v1, 31, v0
	v_lshlrev_b64 v[0:1], 11, v[0:1]
	v_ashrrev_i32_e32 v3, 31, v2
	v_lshl_add_u64 v[38:39], v[8:9], 0, v[0:1]
	v_lshlrev_b64 v[0:1], 11, v[2:3]
	v_lshl_add_u64 v[46:47], v[8:9], 0, v[0:1]
	v_add_co_u32_e32 v0, vcc, s2, v40
	v_ashrrev_i32_e32 v45, 31, v44
	s_nop 0
	v_addc_co_u32_e32 v1, vcc, 0, v41, vcc
	flat_load_dwordx2 v[64:65], v[0:1] nt
	flat_load_dword v74, v[38:39] nt
	flat_load_dword v76, v[46:47] nt
	flat_load_dwordx2 v[62:63], v[0:1] offset:512 nt
	flat_load_dword v80, v[38:39] offset:256 nt
	flat_load_dword v81, v[46:47] offset:256 nt
	flat_load_dwordx2 v[60:61], v[0:1] offset:1024 nt
	flat_load_dword v90, v[38:39] offset:512 nt
	flat_load_dword v91, v[46:47] offset:512 nt
	flat_load_dwordx2 v[58:59], v[0:1] offset:1536 nt
	flat_load_dword v110, v[38:39] offset:768 nt
	flat_load_dword v111, v[46:47] offset:768 nt
	flat_load_dwordx2 v[6:7], v[0:1] offset:2048 nt
	flat_load_dword v69, v[38:39] offset:1024 nt
	flat_load_dword v68, v[46:47] offset:1024 nt
	flat_load_dwordx2 v[4:5], v[0:1] offset:2560 nt
	flat_load_dword v67, v[38:39] offset:1280 nt
	flat_load_dword v66, v[46:47] offset:1280 nt
	flat_load_dwordx2 v[2:3], v[0:1] offset:3072 nt
	flat_load_dword v89, v[38:39] offset:1536 nt
	flat_load_dword v88, v[46:47] offset:1536 nt
	s_nop 0
	flat_load_dwordx2 v[0:1], v[0:1] offset:3584 nt
	s_nop 0
	flat_load_dword v87, v[38:39] offset:1792 nt
	flat_load_dword v86, v[46:47] offset:1792 nt
	v_lshl_add_u64 v[38:39], s[4:5], 0, v[36:37]
	v_lshlrev_b64 v[42:43], 11, v[44:45]
	v_lshl_add_u64 v[72:73], v[8:9], 0, v[42:43]
	v_add_co_u32_e32 v42, vcc, s2, v38
	s_mov_b64 s[2:3], -1
	s_nop 0
	v_addc_co_u32_e32 v43, vcc, 0, v39, vcc
	flat_load_dwordx2 v[56:57], v[42:43] nt
	flat_load_dword v109, v[70:71] nt
	flat_load_dword v108, v[72:73] nt
	flat_load_dwordx2 v[52:53], v[42:43] offset:512 nt
	flat_load_dword v106, v[70:71] offset:256 nt
	flat_load_dword v104, v[72:73] offset:256 nt
	flat_load_dwordx2 v[48:49], v[42:43] offset:1024 nt
	flat_load_dword v101, v[70:71] offset:512 nt
	flat_load_dword v100, v[72:73] offset:512 nt
	flat_load_dwordx2 v[54:55], v[42:43] offset:1536 nt
	flat_load_dword v107, v[70:71] offset:768 nt
	flat_load_dword v105, v[72:73] offset:768 nt
	flat_load_dwordx2 v[50:51], v[42:43] offset:2048 nt
	flat_load_dword v103, v[70:71] offset:1024 nt
	flat_load_dword v102, v[72:73] offset:1024 nt
	flat_load_dwordx2 v[46:47], v[42:43] offset:2560 nt
	flat_load_dword v99, v[70:71] offset:1280 nt
	flat_load_dword v98, v[72:73] offset:1280 nt
	flat_load_dwordx2 v[44:45], v[42:43] offset:3072 nt
	flat_load_dword v97, v[70:71] offset:1536 nt
	flat_load_dword v96, v[72:73] offset:1536 nt
	s_nop 0
	flat_load_dwordx2 v[42:43], v[42:43] offset:3584 nt
	s_nop 0
	flat_load_dword v95, v[70:71] offset:1792 nt
	flat_load_dword v94, v[72:73] offset:1792 nt
	s_and_b64 vcc, exec, s[14:15]
	s_waitcnt vmcnt(0) lgkmcnt(0)
	v_lshlrev_b32_e32 v78, 16, v64
	v_cvt_pk_f32_fp8_e32 v[70:71], v74
	v_cvt_pk_f32_fp8_sdwa v[72:73], v74 src0_sel:WORD_1
	v_cvt_pk_f32_fp8_e32 v[74:75], v76
	v_cvt_pk_f32_fp8_sdwa v[76:77], v76 src0_sel:WORD_1
	v_and_b32_e32 v79, 0xffff0000, v64
	v_lshlrev_b32_e32 v64, 16, v65
	v_pk_add_f32 v[70:71], v[70:71], v[74:75]
	v_and_b32_e32 v65, 0xffff0000, v65
	v_pk_mul_f32 v[70:71], v[70:71], s[72:73] op_sel_hi:[1,0]
	v_cvt_pk_f32_fp8_sdwa v[74:75], v81 src0_sel:WORD_1
	v_pk_fma_f32 v[82:83], v[78:79], s[90:91], v[70:71] op_sel_hi:[1,0,1]
	v_pk_add_f32 v[70:71], v[72:73], v[76:77]
	v_cvt_pk_f32_fp8_e32 v[72:73], v81
	v_pk_mul_f32 v[70:71], v[70:71], s[72:73] op_sel_hi:[1,0]
	v_lshlrev_b32_e32 v76, 16, v62
	v_pk_fma_f32 v[84:85], v[64:65], s[90:91], v[70:71] op_sel_hi:[1,0,1]
	v_add_f32_e32 v65, v82, v83
	v_add_f32_e32 v64, v85, v84
	v_add_f32_e32 v64, v65, v64
	v_add_f32_e32 v78, 0, v64
	v_cvt_pk_f32_fp8_e32 v[64:65], v80
	v_cvt_pk_f32_fp8_sdwa v[70:71], v80 src0_sel:WORD_1
	v_and_b32_e32 v77, 0xffff0000, v62
	v_lshlrev_b32_e32 v62, 16, v63
	v_pk_add_f32 v[64:65], v[64:65], v[72:73]
	v_pk_add_f32 v[70:71], v[70:71], v[74:75]
	v_pk_mul_f32 v[64:65], v[64:65], s[72:73] op_sel_hi:[1,0]
	v_and_b32_e32 v63, 0xffff0000, v63
	v_pk_mul_f32 v[70:71], v[70:71], s[72:73] op_sel_hi:[1,0]
	v_pk_fma_f32 v[64:65], v[76:77], s[90:91], v[64:65] op_sel_hi:[1,0,1]
	v_pk_fma_f32 v[80:81], v[62:63], s[90:91], v[70:71] op_sel_hi:[1,0,1]
	v_add_f32_e32 v63, v64, v65
	v_add_f32_e32 v62, v81, v80
	v_add_f32_e32 v62, v63, v62
	v_add_f32_e32 v112, v78, v62
	v_cvt_pk_f32_fp8_e32 v[62:63], v90
	v_cvt_pk_f32_fp8_e32 v[72:73], v91
	v_cvt_pk_f32_fp8_sdwa v[70:71], v90 src0_sel:WORD_1
	v_cvt_pk_f32_fp8_sdwa v[74:75], v91 src0_sel:WORD_1
	v_lshlrev_b32_e32 v76, 16, v60
	v_pk_add_f32 v[62:63], v[62:63], v[72:73]
; __device__ __forceinline__ float bflo(unsigned w) { return __uint_as_float(w << 16); }
; __device__ __forceinline__ float bfhi(unsigned w) { return __uint_as_float(w & 0xffff0000u); }
; __global__ void __launch_bounds__(NTHREADS, 2) hybrid_fwd(Args a) {
;     ...
;                     for (int j = 0; j < 8; ++j) { const u32x2 x = xw[rr][j]; const int p = (int)pw_[rr][j], q = (int)qw[rr][j];
;                         const f32x2 p0 = __builtin_amdgcn_cvt_pk_f32_fp8(p, false), p1 = __builtin_amdgcn_cvt_pk_f32_fp8(p, true), q0 = __builtin_amdgcn_cvt_pk_f32_fp8(q, false), q1 = __builtin_amdgcn_cvt_pk_f32_fp8(q, true);
;                         y[j][0] = bflo(x.x) * ALPHA + (p0.x + q0.x) * (1.f / Y2_SCALE); y[j][1] = bfhi(x.x) * ALPHA + (p0.y + q0.y) * (1.f / Y2_SCALE);
;                         y[j][2] = bflo(x.y) * ALPHA + (p1.x + q1.x) * (1.f / Y2_SCALE); y[j][3] = bfhi(x.y) * ALPHA + (p1.y + q1.y) * (1.f / Y2_SCALE);
;                         s += (y[j][0] + y[j][1]) + (y[j][2] + y[j][3]); }
	v_and_b32_e32 v77, 0xffff0000, v60
	v_pk_mul_f32 v[62:63], v[62:63], s[72:73] op_sel_hi:[1,0]
	v_lshlrev_b32_e32 v60, 16, v61
	v_pk_fma_f32 v[72:73], v[76:77], s[90:91], v[62:63] op_sel_hi:[1,0,1]
	v_pk_add_f32 v[62:63], v[70:71], v[74:75]
	v_and_b32_e32 v61, 0xffff0000, v61
	v_pk_mul_f32 v[62:63], v[62:63], s[72:73] op_sel_hi:[1,0]
	v_cvt_pk_f32_fp8_e32 v[70:71], v111
	v_pk_fma_f32 v[78:79], v[60:61], s[90:91], v[62:63] op_sel_hi:[1,0,1]
	v_add_f32_e32 v61, v72, v73
	v_add_f32_e32 v60, v79, v78
	v_add_f32_e32 v60, v61, v60
	v_add_f32_e32 v90, v112, v60
	v_cvt_pk_f32_fp8_e32 v[60:61], v110
	v_cvt_pk_f32_fp8_sdwa v[62:63], v110 src0_sel:WORD_1
	v_cvt_pk_f32_fp8_sdwa v[74:75], v111 src0_sel:WORD_1
	v_lshlrev_b32_e32 v76, 16, v58
	v_pk_add_f32 v[60:61], v[60:61], v[70:71]
	v_and_b32_e32 v77, 0xffff0000, v58
	v_pk_mul_f32 v[60:61], v[60:61], s[72:73] op_sel_hi:[1,0]
	v_lshlrev_b32_e32 v58, 16, v59
	v_pk_fma_f32 v[70:71], v[76:77], s[90:91], v[60:61] op_sel_hi:[1,0,1]
	v_pk_add_f32 v[60:61], v[62:63], v[74:75]
	v_and_b32_e32 v59, 0xffff0000, v59
	v_pk_mul_f32 v[60:61], v[60:61], s[72:73] op_sel_hi:[1,0]
	v_cvt_pk_f32_fp8_e32 v[62:63], v68
	v_pk_fma_f32 v[76:77], v[58:59], s[90:91], v[60:61] op_sel_hi:[1,0,1]
	v_add_f32_e32 v59, v70, v71
	v_add_f32_e32 v58, v77, v76
	v_add_f32_e32 v58, v59, v58
	v_add_f32_e32 v90, v90, v58
	v_cvt_pk_f32_fp8_e32 v[58:59], v69
	v_cvt_pk_f32_fp8_sdwa v[60:61], v69 src0_sel:WORD_1
	v_cvt_pk_f32_fp8_sdwa v[74:75], v68 src0_sel:WORD_1
	v_lshlrev_b32_e32 v68, 16, v6
	v_pk_add_f32 v[58:59], v[58:59], v[62:63]
	v_and_b32_e32 v69, 0xffff0000, v6
	v_pk_mul_f32 v[58:59], v[58:59], s[72:73] op_sel_hi:[1,0]
	v_lshlrev_b32_e32 v6, 16, v7
	v_pk_fma_f32 v[68:69], v[68:69], s[90:91], v[58:59] op_sel_hi:[1,0,1]
	v_pk_add_f32 v[58:59], v[60:61], v[74:75]
	v_and_b32_e32 v7, 0xffff0000, v7
	v_pk_mul_f32 v[58:59], v[58:59], s[72:73] op_sel_hi:[1,0]
	v_cvt_pk_f32_fp8_e32 v[60:61], v66
	v_pk_fma_f32 v[74:75], v[6:7], s[90:91], v[58:59] op_sel_hi:[1,0,1]
	v_add_f32_e32 v7, v68, v69
	v_add_f32_e32 v6, v75, v74
	v_add_f32_e32 v6, v7, v6
	v_add_f32_e32 v90, v90, v6
	v_cvt_pk_f32_fp8_e32 v[6:7], v67
	v_cvt_pk_f32_fp8_sdwa v[58:59], v67 src0_sel:WORD_1
	v_cvt_pk_f32_fp8_sdwa v[66:67], v66 src0_sel:WORD_1
	v_lshlrev_b32_e32 v62, 16, v4
	v_pk_add_f32 v[6:7], v[6:7], v[60:61]
	v_and_b32_e32 v63, 0xffff0000, v4
	v_pk_mul_f32 v[6:7], v[6:7], s[72:73] op_sel_hi:[1,0]
	v_lshlrev_b32_e32 v4, 16, v5
	v_pk_fma_f32 v[62:63], v[62:63], s[90:91], v[6:7] op_sel_hi:[1,0,1]
	v_pk_add_f32 v[6:7], v[58:59], v[66:67]
	v_and_b32_e32 v5, 0xffff0000, v5
	v_pk_mul_f32 v[6:7], v[6:7], s[72:73] op_sel_hi:[1,0]
	v_cvt_pk_f32_fp8_e32 v[58:59], v88
	v_pk_fma_f32 v[66:67], v[4:5], s[90:91], v[6:7] op_sel_hi:[1,0,1]
	v_add_f32_e32 v5, v62, v63
	v_add_f32_e32 v4, v67, v66
	v_add_f32_e32 v4, v5, v4
	v_add_f32_e32 v90, v90, v4
	v_cvt_pk_f32_fp8_e32 v[4:5], v89
	v_cvt_pk_f32_fp8_sdwa v[6:7], v89 src0_sel:WORD_1
	v_cvt_pk_f32_fp8_sdwa v[60:61], v88 src0_sel:WORD_1
	v_lshlrev_b32_e32 v88, 16, v2
	v_pk_add_f32 v[4:5], v[4:5], v[58:59]
	v_and_b32_e32 v89, 0xffff0000, v2
	v_pk_mul_f32 v[4:5], v[4:5], s[72:73] op_sel_hi:[1,0]
	v_lshlrev_b32_e32 v2, 16, v3
	v_pk_fma_f32 v[58:59], v[88:89], s[90:91], v[4:5] op_sel_hi:[1,0,1]
	v_pk_add_f32 v[4:5], v[6:7], v[60:61]
	v_and_b32_e32 v3, 0xffff0000, v3
	v_pk_mul_f32 v[4:5], v[4:5], s[72:73] op_sel_hi:[1,0]
	v_cvt_pk_f32_fp8_e32 v[88:89], v86
	v_pk_fma_f32 v[60:61], v[2:3], s[90:91], v[4:5] op_sel_hi:[1,0,1]
	v_add_f32_e32 v3, v58, v59
	v_add_f32_e32 v2, v61, v60
	v_cvt_pk_f32_fp8_e32 v[4:5], v87
	v_add_f32_e32 v2, v3, v2
	v_add_f32_e32 v2, v90, v2
	v_cvt_pk_f32_fp8_sdwa v[6:7], v87 src0_sel:WORD_1
	v_cvt_pk_f32_fp8_sdwa v[90:91], v86 src0_sel:WORD_1
	v_pk_add_f32 v[4:5], v[4:5], v[88:89]
	v_lshlrev_b32_e32 v86, 16, v0
	v_and_b32_e32 v87, 0xffff0000, v0
	v_pk_mul_f32 v[4:5], v[4:5], s[72:73] op_sel_hi:[1,0]
	v_lshlrev_b32_e32 v0, 16, v1
	v_pk_fma_f32 v[86:87], v[86:87], s[90:91], v[4:5] op_sel_hi:[1,0,1]
	v_pk_add_f32 v[4:5], v[6:7], v[90:91]
	v_and_b32_e32 v1, 0xffff0000, v1
	v_pk_mul_f32 v[4:5], v[4:5], s[72:73] op_sel_hi:[1,0]
	s_nop 0
	v_pk_fma_f32 v[88:89], v[0:1], s[90:91], v[4:5] op_sel_hi:[1,0,1]
	v_add_f32_e32 v1, v86, v87
; __device__ __forceinline__ unsigned cvt_pk_bf16(float lo, float hi) { unsigned r; asm volatile("v_cvt_pk_bf16_f32 %0, %1, %2" : "=v"(r) : "v"(lo), "v"(hi)); return r; }
; __global__ void __launch_bounds__(NTHREADS, 2) hybrid_fwd(Args a) {
;     ...
;                     const float mean = wave_sum(s) * (1.f / DM); float s2 = 0.f;
; #pragma unroll
;                     for (int j = 0; j < 8; ++j) { y[j] = y[j] - mean; s2 += (y[j][0] * y[j][0] + y[j][1] * y[j][1]) + (y[j][2] * y[j][2] + y[j][3] * y[j][3]); }
;                     const float rstd = __builtin_amdgcn_rsqf(wave_sum(s2) * (1.f / DM) + LN_EPS);
; #pragma unroll
;                     for (int j = 0; j < 8; ++j) { const f32x4 gg = *(const f32x4*)(lg + j * 256 + lane * 4), bb = *(const f32x4*)(lb + j * 256 + lane * 4);
;                         y[j] = y[j] * rstd * gg + bb;
;                         if (lastl) __builtin_nontemporal_store(y[j], (f32x4*)(a.out + (size_t)row * DM + j * 256 + lane * 4));
;                         else { u32x2 w; w.x = cvt_pk_bf16(y[j][0], y[j][1]); w.y = cvt_pk_bf16(y[j][2], y[j][3]); __builtin_nontemporal_store(w, (u32x2*)(XA16 + (size_t)row * DM + j * 256 + lane * 4)); }
	v_add_f32_e32 v0, v89, v88
	v_add_f32_e32 v0, v1, v0
	v_add_f32_e32 v0, v2, v0
	s_nop 1
	v_add_f32_dpp v0, v0, v0 quad_perm:[1,0,3,2] row_mask:0xf bank_mask:0xf bound_ctrl:1
	s_nop 1
	v_add_f32_dpp v0, v0, v0 quad_perm:[2,3,0,1] row_mask:0xf bank_mask:0xf bound_ctrl:1
	s_nop 1
	v_add_f32_dpp v0, v0, v0 row_ror:4 row_mask:0xf bank_mask:0xf bound_ctrl:1
	s_nop 1
	v_add_f32_dpp v0, v0, v0 row_ror:8 row_mask:0xf bank_mask:0xf bound_ctrl:1
	v_mov_b32_e32 v1, v0
	s_nop 1
	v_permlane16_swap_b32_e32 v0, v1
	v_add_f32_e32 v0, v0, v1
	v_mov_b32_e32 v1, v0
	s_nop 1
	v_permlane32_swap_b32_e32 v0, v1
	v_add_f32_e32 v0, v0, v1
	v_fmac_f32_e32 v85, 0xba000000, v0
	v_fmac_f32_e32 v83, 0xba000000, v0
	v_fmamk_f32 v84, v0, 0xba000000, v84
	v_fmamk_f32 v82, v0, 0xba000000, v82
	v_mul_f32_e32 v1, v83, v83
	v_mul_f32_e32 v2, v85, v85
	v_fmac_f32_e32 v1, v82, v82
	v_fmac_f32_e32 v2, v84, v84
	v_fmamk_f32 v81, v0, 0xba000000, v81
	v_fmamk_f32 v65, v0, 0xba000000, v65
	v_add_f32_e32 v1, v1, v2
	v_fmac_f32_e32 v80, 0xba000000, v0
	v_fmac_f32_e32 v64, 0xba000000, v0
	v_mul_f32_e32 v2, v65, v65
	v_mul_f32_e32 v3, v81, v81
	v_fmac_f32_e32 v2, v64, v64
	v_fmac_f32_e32 v3, v80, v80
	v_add_f32_e32 v2, v2, v3
	v_fmamk_f32 v79, v0, 0xba000000, v79
	v_fmamk_f32 v73, v0, 0xba000000, v73
	v_add_f32_e32 v1, v1, v2
	v_fmac_f32_e32 v78, 0xba000000, v0
	v_fmac_f32_e32 v72, 0xba000000, v0
	v_mul_f32_e32 v2, v73, v73
	v_mul_f32_e32 v3, v79, v79
	v_fmac_f32_e32 v2, v72, v72
	v_fmac_f32_e32 v3, v78, v78
	v_add_f32_e32 v2, v2, v3
	v_fmamk_f32 v77, v0, 0xba000000, v77
	v_fmamk_f32 v71, v0, 0xba000000, v71
	v_add_f32_e32 v1, v1, v2
	v_fmac_f32_e32 v76, 0xba000000, v0
	v_fmac_f32_e32 v70, 0xba000000, v0
	v_mul_f32_e32 v2, v71, v71
	v_mul_f32_e32 v3, v77, v77
	v_fmac_f32_e32 v2, v70, v70
	v_fmac_f32_e32 v3, v76, v76
	v_add_f32_e32 v2, v2, v3
	v_fmamk_f32 v75, v0, 0xba000000, v75
	v_fmamk_f32 v69, v0, 0xba000000, v69
	v_add_f32_e32 v1, v1, v2
	v_fmac_f32_e32 v74, 0xba000000, v0
	v_fmac_f32_e32 v68, 0xba000000, v0
	v_mul_f32_e32 v2, v69, v69
	v_mul_f32_e32 v3, v75, v75
	v_fmac_f32_e32 v2, v68, v68
	v_fmac_f32_e32 v3, v74, v74
	v_add_f32_e32 v2, v2, v3
	v_fmamk_f32 v67, v0, 0xba000000, v67
	v_fmamk_f32 v63, v0, 0xba000000, v63
	v_add_f32_e32 v1, v1, v2
	v_fmac_f32_e32 v66, 0xba000000, v0
	v_fmac_f32_e32 v62, 0xba000000, v0
	v_mul_f32_e32 v2, v63, v63
	v_mul_f32_e32 v3, v67, v67
	v_fmac_f32_e32 v2, v62, v62
	v_fmac_f32_e32 v3, v66, v66
	v_add_f32_e32 v2, v2, v3
	v_fmamk_f32 v61, v0, 0xba000000, v61
	v_fmamk_f32 v59, v0, 0xba000000, v59
	v_add_f32_e32 v1, v1, v2
	v_fmac_f32_e32 v60, 0xba000000, v0
	v_fmac_f32_e32 v58, 0xba000000, v0
	v_mul_f32_e32 v2, v59, v59
	v_mul_f32_e32 v3, v61, v61
	v_fmac_f32_e32 v2, v58, v58
	v_fmac_f32_e32 v3, v60, v60
	v_add_f32_e32 v2, v2, v3
	v_fmamk_f32 v89, v0, 0xba000000, v89
	v_fmamk_f32 v87, v0, 0xba000000, v87
	v_add_f32_e32 v1, v1, v2
	v_fmac_f32_e32 v88, 0xba000000, v0
	v_fmac_f32_e32 v86, 0xba000000, v0
	v_mul_f32_e32 v0, v87, v87
	v_mul_f32_e32 v2, v89, v89
	v_fmac_f32_e32 v0, v86, v86
	v_fmac_f32_e32 v2, v88, v88
	v_add_f32_e32 v0, v0, v2
	v_add_f32_e32 v0, v1, v0
	s_nop 1
	v_add_f32_dpp v0, v0, v0 quad_perm:[1,0,3,2] row_mask:0xf bank_mask:0xf bound_ctrl:1
	s_nop 1
	v_add_f32_dpp v0, v0, v0 quad_perm:[2,3,0,1] row_mask:0xf bank_mask:0xf bound_ctrl:1
	s_nop 1
	v_add_f32_dpp v0, v0, v0 row_ror:4 row_mask:0xf bank_mask:0xf bound_ctrl:1
	s_nop 1
	v_add_f32_dpp v0, v0, v0 row_ror:8 row_mask:0xf bank_mask:0xf bound_ctrl:1
	v_mov_b32_e32 v1, v0
	s_nop 1
	v_permlane16_swap_b32_e32 v0, v1
	v_add_f32_e32 v0, v0, v1
	v_mov_b32_e32 v1, v0
	s_nop 1
	v_permlane32_swap_b32_e32 v0, v1
	v_add_f32_e32 v0, v0, v1
	v_fmamk_f32 v0, v0, 0x3a000000, v207
	v_rsq_f32_e32 v90, v0
	s_nop 0
	v_pk_mul_f32 v[82:83], v[90:91], v[82:83] op_sel_hi:[0,1]
	v_pk_mul_f32 v[84:85], v[90:91], v[84:85] op_sel_hi:[0,1]
	v_pk_fma_f32 v[2:3], v[84:85], v[154:155], v[190:191]
	v_pk_fma_f32 v[0:1], v[82:83], v[152:153], v[188:189]
	s_cbranch_vccz .LBB0_1338
	v_add_co_u32_e32 v6, vcc, 0x38000000, v40
	v_cvt_pk_bf16_f32 v4, v0, v1
	v_cvt_pk_bf16_f32 v5, v2, v3
	s_mov_b64 s[2:3], 0
	s_nop 0
	v_addc_co_u32_e32 v7, vcc, 0, v41, vcc
	flat_store_dwordx2 v[6:7], v[4:5] nt
